# topk radix select: wave-parallel DPP suffix-scan threshold-bin search replaces single-thread serial LDS walk (4 passes)
# speedup vs baseline: 1.0561x; 1.0292x over previous
; __device__ __forceinline__ void phase_topk(const Args& a, const Ctx& c0, int l, bool last) {
;     ...
;         unsigned prefix = 0u, mask = 0u, want = (unsigned)cap;
;         for (int pass = 0; pass < 4; ++pass) { const int shift = 24 - 8 * pass;
;             if (tid < 256) hist[tid] = 0u;
;             __syncthreads();
; #pragma unroll
;             for (int j = 0; j < 8; ++j) if ((k[j] & mask) == prefix) atomicAdd((unsigned*)&hist[(k[j] >> shift) & 255u], 1u);
;             __syncthreads();
;             if (tid == 0) { unsigned cum = 0u; int d = 255; for (; d > 0; --d) { const unsigned hh = hist[d]; if (cum + hh >= want) break; cum += hh; } misc[0] = (unsigned)d; misc[1] = want - cum; }
;             __syncthreads();
;             prefix |= misc[0] << shift; mask |= 255u << shift; want = misc[1];
.LBB0_2104:
	s_or_b64 exec, exec, s[2:3]
	s_waitcnt vmcnt(0)
	v_lshrrev_b32_e32 v1, 24, v11
	v_lshl_add_u32 v1, v1, 2, 0
	s_waitcnt lgkmcnt(0)
	s_barrier
	ds_add_u32 v1, v181
	v_lshrrev_b32_e32 v1, 24, v10
	v_lshl_add_u32 v1, v1, 2, 0
	ds_add_u32 v1, v181
	v_lshrrev_b32_e32 v1, 24, v9
	v_lshl_add_u32 v1, v1, 2, 0
	ds_add_u32 v1, v181
	v_lshrrev_b32_e32 v1, 24, v8
	v_lshl_add_u32 v1, v1, 2, 0
	ds_add_u32 v1, v181
	v_lshrrev_b32_e32 v1, 24, v7
	v_lshl_add_u32 v1, v1, 2, 0
	ds_add_u32 v1, v181
	v_lshrrev_b32_e32 v1, 24, v6
	v_lshl_add_u32 v1, v1, 2, 0
	ds_add_u32 v1, v181
	v_lshrrev_b32_e32 v1, 24, v5
	v_lshl_add_u32 v1, v1, 2, 0
	ds_add_u32 v1, v181
	v_lshrrev_b32_e32 v1, 24, v4
	v_lshl_add_u32 v1, v1, 2, 0
	ds_add_u32 v1, v181
	s_waitcnt lgkmcnt(0)
	s_barrier
	s_and_saveexec_b64 s[2:3], s[40:41]
	s_cbranch_execz .LBB0_2129
	s_and_b64 s[4:5], s[24:25], exec
	s_cselect_b32 s18, 32, 0x200
	s_mov_b64 exec, -1
	v_mbcnt_lo_u32_b32 v102, -1, 0
	v_mbcnt_hi_u32_b32 v102, -1, v102
	v_lshlrev_b32_e32 v102, 4, v102
	ds_read_b128 v[104:107], v102
	s_waitcnt lgkmcnt(0)
	v_add_u32_e32 v108, v104, v105
	v_add3_u32 v108, v108, v106, v107
	s_nop 1
	v_add_u32_dpp v108, v108, v108 row_shl:1 row_mask:0xf bank_mask:0xf
	s_nop 1
	v_add_u32_dpp v108, v108, v108 row_shl:2 row_mask:0xf bank_mask:0xf
	s_nop 1
	v_add_u32_dpp v108, v108, v108 row_shl:4 row_mask:0xf bank_mask:0xf
	s_nop 1
	v_add_u32_dpp v108, v108, v108 row_shl:8 row_mask:0xf bank_mask:0xf
	s_nop 0
	v_readlane_b32 s5, v108, 16
	v_readlane_b32 s6, v108, 32
	v_readlane_b32 s7, v108, 48
	s_add_i32 s6, s6, s7
	s_add_i32 s5, s5, s6
	s_mov_b32 exec_lo, 0xffff
	s_mov_b32 exec_hi, 0
	v_add_u32_e32 v108, s5, v108
	s_mov_b32 exec_lo, 0xffff0000
	v_add_u32_e32 v108, s6, v108
	s_mov_b32 exec_lo, 0
	s_mov_b32 exec_hi, 0xffff
	v_add_u32_e32 v108, s7, v108
	s_mov_b64 exec, -1
	v_sub_u32_e32 v109, v108, v104
	v_sub_u32_e32 v110, v109, v105
	v_sub_u32_e32 v111, v110, v106
	v_cmp_le_u32_e64 s[4:5], s18, v108
	v_cmp_le_u32_e64 s[6:7], s18, v109
	v_cmp_le_u32_e64 s[8:9], s18, v110
	v_cmp_le_u32_e64 s[10:11], s18, v111
	s_andn2_b64 s[4:5], s[4:5], 1
	s_bcnt1_i32_b64 s4, s[4:5]
	s_bcnt1_i32_b64 s6, s[6:7]
	s_bcnt1_i32_b64 s8, s[8:9]
	s_bcnt1_i32_b64 s10, s[10:11]
	s_add_i32 s4, s4, s6
	s_add_i32 s8, s8, s10
	s_add_i32 s48, s4, s8
	s_add_i32 s5, s48, 1
	s_lshr_b32 s6, s5, 2
	s_and_b32 s7, s5, 3
	s_min_u32 s6, s6, 63
	v_readlane_b32 s8, v108, s6
	v_readlane_b32 s9, v109, s6
	v_readlane_b32 s10, v110, s6
	v_readlane_b32 s11, v111, s6
	s_cmp_eq_u32 s7, 1
	s_cselect_b32 s8, s9, s8
	s_cmp_eq_u32 s7, 2
	s_cselect_b32 s8, s10, s8
	s_cmp_eq_u32 s7, 3
	s_cselect_b32 s8, s11, s8
	s_cmp_gt_u32 s5, 0xff
	s_cselect_b32 s8, 0, s8
	s_sub_i32 s4, s18, s8
	s_mov_b64 exec, 1
	v_mov_b32_e32 v2, s48
	v_mov_b32_e32 v3, s4
	ds_write_b64 v147, v[2:3] offset:1024
	s_branch .LBB0_2129

; __device__ __forceinline__ void phase_topk(const Args& a, const Ctx& c0, int l, bool last) {
;     ...
;         for (int pass = 0; pass < 4; ++pass) { const int shift = 24 - 8 * pass;
;             if (tid < 256) hist[tid] = 0u;
;             __syncthreads();
; #pragma unroll
;             for (int j = 0; j < 8; ++j) if ((k[j] & mask) == prefix) atomicAdd((unsigned*)&hist[(k[j] >> shift) & 255u], 1u);
;             __syncthreads();
;             if (tid == 0) { unsigned cum = 0u; int d = 255; for (; d > 0; --d) { const unsigned hh = hist[d]; if (cum + hh >= want) break; cum += hh; } misc[0] = (unsigned)d; misc[1] = want - cum; }
;             __syncthreads();
;             prefix |= misc[0] << shift; mask |= 255u << shift; want = misc[1];
.LBB0_2129:
	s_or_b64 exec, exec, s[2:3]
	s_waitcnt lgkmcnt(0)
	s_barrier
	ds_read_b64 v[2:3], v147 offset:1024
	s_waitcnt lgkmcnt(0)
	s_barrier
	v_readfirstlane_b32 s4, v2
	v_readfirstlane_b32 s19, v3
	s_and_saveexec_b64 s[2:3], s[38:39]
	ds_write_b32 v45, v147
	s_or_b64 exec, exec, s[2:3]
	s_lshl_b32 s18, s4, 24
	v_and_b32_e32 v1, 0xff000000, v11
	v_cmp_eq_u32_e32 vcc, s18, v1
	s_waitcnt lgkmcnt(0)
	s_barrier
	s_and_saveexec_b64 s[2:3], vcc
	v_bfe_u32 v1, v11, 16, 8
	v_lshl_add_u32 v1, v1, 2, 0
	ds_add_u32 v1, v181
	s_or_b64 exec, exec, s[2:3]
	v_and_b32_e32 v1, 0xff000000, v10
	v_cmp_eq_u32_e32 vcc, s18, v1
	s_and_saveexec_b64 s[2:3], vcc
	v_bfe_u32 v1, v10, 16, 8
	v_lshl_add_u32 v1, v1, 2, 0
	ds_add_u32 v1, v181
	s_or_b64 exec, exec, s[2:3]
	v_and_b32_e32 v1, 0xff000000, v9
	v_cmp_eq_u32_e32 vcc, s18, v1
	s_and_saveexec_b64 s[2:3], vcc
	v_bfe_u32 v1, v9, 16, 8
	v_lshl_add_u32 v1, v1, 2, 0
	ds_add_u32 v1, v181
	s_or_b64 exec, exec, s[2:3]
	v_and_b32_e32 v1, 0xff000000, v8
	v_cmp_eq_u32_e32 vcc, s18, v1
	s_and_saveexec_b64 s[2:3], vcc
	v_bfe_u32 v1, v8, 16, 8
	v_lshl_add_u32 v1, v1, 2, 0
	ds_add_u32 v1, v181
	s_or_b64 exec, exec, s[2:3]
	v_and_b32_e32 v1, 0xff000000, v7
	v_cmp_eq_u32_e32 vcc, s18, v1
	s_and_saveexec_b64 s[2:3], vcc
	v_bfe_u32 v1, v7, 16, 8
	v_lshl_add_u32 v1, v1, 2, 0
	ds_add_u32 v1, v181
	s_or_b64 exec, exec, s[2:3]
	v_and_b32_e32 v1, 0xff000000, v6
	v_cmp_eq_u32_e32 vcc, s18, v1
	s_and_saveexec_b64 s[2:3], vcc
	v_bfe_u32 v1, v6, 16, 8
	v_lshl_add_u32 v1, v1, 2, 0
	ds_add_u32 v1, v181
	s_or_b64 exec, exec, s[2:3]
	v_and_b32_e32 v1, 0xff000000, v5
	v_cmp_eq_u32_e32 vcc, s18, v1
	s_and_saveexec_b64 s[2:3], vcc
	v_bfe_u32 v1, v5, 16, 8
	v_lshl_add_u32 v1, v1, 2, 0
	ds_add_u32 v1, v181
	s_or_b64 exec, exec, s[2:3]
	v_and_b32_e32 v1, 0xff000000, v4
	v_cmp_eq_u32_e32 vcc, s18, v1
	s_and_saveexec_b64 s[2:3], vcc
	v_bfe_u32 v1, v4, 16, 8
	v_lshl_add_u32 v1, v1, 2, 0
	ds_add_u32 v1, v181
	s_or_b64 exec, exec, s[2:3]
	s_waitcnt lgkmcnt(0)
	s_barrier
	s_and_saveexec_b64 s[2:3], s[40:41]
	s_cbranch_execz .LBB0_2170
	s_mov_b64 exec, -1
	v_mbcnt_lo_u32_b32 v102, -1, 0
	v_mbcnt_hi_u32_b32 v102, -1, v102
	v_lshlrev_b32_e32 v102, 4, v102
	ds_read_b128 v[104:107], v102
	s_waitcnt lgkmcnt(0)
	v_add_u32_e32 v108, v104, v105
	v_add3_u32 v108, v108, v106, v107
	s_nop 1
	v_add_u32_dpp v108, v108, v108 row_shl:1 row_mask:0xf bank_mask:0xf
	s_nop 1
	v_add_u32_dpp v108, v108, v108 row_shl:2 row_mask:0xf bank_mask:0xf
	s_nop 1
	v_add_u32_dpp v108, v108, v108 row_shl:4 row_mask:0xf bank_mask:0xf
	s_nop 1
	v_add_u32_dpp v108, v108, v108 row_shl:8 row_mask:0xf bank_mask:0xf
	s_nop 0
	v_readlane_b32 s5, v108, 16
	v_readlane_b32 s6, v108, 32
	v_readlane_b32 s7, v108, 48
	s_add_i32 s6, s6, s7
	s_add_i32 s5, s5, s6
	s_mov_b32 exec_lo, 0xffff
	s_mov_b32 exec_hi, 0
	v_add_u32_e32 v108, s5, v108
	s_mov_b32 exec_lo, 0xffff0000
	v_add_u32_e32 v108, s6, v108
	s_mov_b32 exec_lo, 0
	s_mov_b32 exec_hi, 0xffff
	v_add_u32_e32 v108, s7, v108
	s_mov_b64 exec, -1
	v_sub_u32_e32 v109, v108, v104
	v_sub_u32_e32 v110, v109, v105
	v_sub_u32_e32 v111, v110, v106
	v_cmp_le_u32_e64 s[4:5], s19, v108
	v_cmp_le_u32_e64 s[6:7], s19, v109
	v_cmp_le_u32_e64 s[8:9], s19, v110
	v_cmp_le_u32_e64 s[10:11], s19, v111
	s_andn2_b64 s[4:5], s[4:5], 1
	s_bcnt1_i32_b64 s4, s[4:5]
	s_bcnt1_i32_b64 s6, s[6:7]
	s_bcnt1_i32_b64 s8, s[8:9]
	s_bcnt1_i32_b64 s10, s[10:11]
	s_add_i32 s4, s4, s6
	s_add_i32 s8, s8, s10
	s_add_i32 s48, s4, s8
	s_add_i32 s5, s48, 1
	s_lshr_b32 s6, s5, 2
	s_and_b32 s7, s5, 3
	s_min_u32 s6, s6, 63
	v_readlane_b32 s8, v108, s6
	v_readlane_b32 s9, v109, s6
	v_readlane_b32 s10, v110, s6
	v_readlane_b32 s11, v111, s6
	s_cmp_eq_u32 s7, 1
	s_cselect_b32 s8, s9, s8
	s_cmp_eq_u32 s7, 2
	s_cselect_b32 s8, s10, s8
	s_cmp_eq_u32 s7, 3
	s_cselect_b32 s8, s11, s8
	s_cmp_gt_u32 s5, 0xff
	s_cselect_b32 s8, 0, s8
	s_sub_i32 s4, s19, s8
	s_mov_b64 exec, 1
	v_mov_b32_e32 v2, s48
	v_mov_b32_e32 v3, s4
	ds_write_b64 v147, v[2:3] offset:1024
.LBB0_2170:
	s_or_b64 exec, exec, s[2:3]
	s_waitcnt lgkmcnt(0)
	s_barrier
	ds_read_b64 v[2:3], v147 offset:1024
	s_waitcnt lgkmcnt(0)
	s_barrier
	v_readfirstlane_b32 s4, v2
	v_readfirstlane_b32 s19, v3
	s_and_saveexec_b64 s[2:3], s[38:39]
	ds_write_b32 v45, v147
	s_or_b64 exec, exec, s[2:3]
	s_lshl_b32 s2, s4, 16
	s_or_b32 s18, s2, s18
	v_and_b32_e32 v1, 0xffff0000, v11
	v_cmp_eq_u32_e32 vcc, s18, v1
	s_waitcnt lgkmcnt(0)
	s_barrier
	s_and_saveexec_b64 s[2:3], vcc
	v_bfe_u32 v1, v11, 8, 8
	v_lshl_add_u32 v1, v1, 2, 0
	ds_add_u32 v1, v181
	s_or_b64 exec, exec, s[2:3]
	v_and_b32_e32 v1, 0xffff0000, v10
	v_cmp_eq_u32_e32 vcc, s18, v1
	s_and_saveexec_b64 s[2:3], vcc
	v_bfe_u32 v1, v10, 8, 8
	v_lshl_add_u32 v1, v1, 2, 0
	ds_add_u32 v1, v181
	s_or_b64 exec, exec, s[2:3]
	v_and_b32_e32 v1, 0xffff0000, v9
	v_cmp_eq_u32_e32 vcc, s18, v1
	s_and_saveexec_b64 s[2:3], vcc
	v_bfe_u32 v1, v9, 8, 8
	v_lshl_add_u32 v1, v1, 2, 0
	ds_add_u32 v1, v181
	s_or_b64 exec, exec, s[2:3]
	v_and_b32_e32 v1, 0xffff0000, v8
	v_cmp_eq_u32_e32 vcc, s18, v1
	s_and_saveexec_b64 s[2:3], vcc
	v_bfe_u32 v1, v8, 8, 8
	v_lshl_add_u32 v1, v1, 2, 0
	ds_add_u32 v1, v181
	s_or_b64 exec, exec, s[2:3]
	v_and_b32_e32 v1, 0xffff0000, v7
	v_cmp_eq_u32_e32 vcc, s18, v1
	s_and_saveexec_b64 s[2:3], vcc
	v_bfe_u32 v1, v7, 8, 8
	v_lshl_add_u32 v1, v1, 2, 0
	ds_add_u32 v1, v181
	s_or_b64 exec, exec, s[2:3]
	v_and_b32_e32 v1, 0xffff0000, v6
	v_cmp_eq_u32_e32 vcc, s18, v1
	s_and_saveexec_b64 s[2:3], vcc
	v_bfe_u32 v1, v6, 8, 8
	v_lshl_add_u32 v1, v1, 2, 0
	ds_add_u32 v1, v181
	s_or_b64 exec, exec, s[2:3]
	v_and_b32_e32 v1, 0xffff0000, v5
	v_cmp_eq_u32_e32 vcc, s18, v1
	s_and_saveexec_b64 s[2:3], vcc
	v_bfe_u32 v1, v5, 8, 8
	v_lshl_add_u32 v1, v1, 2, 0
	ds_add_u32 v1, v181
	s_or_b64 exec, exec, s[2:3]
	v_and_b32_e32 v1, 0xffff0000, v4
	v_cmp_eq_u32_e32 vcc, s18, v1
	s_and_saveexec_b64 s[2:3], vcc
	v_bfe_u32 v1, v4, 8, 8
	v_lshl_add_u32 v1, v1, 2, 0
	ds_add_u32 v1, v181
	s_or_b64 exec, exec, s[2:3]
	s_waitcnt lgkmcnt(0)
	s_barrier
; __device__ __forceinline__ void phase_topk(const Args& a, const Ctx& c0, int l, bool last) {
;     ...
;         for (int pass = 0; pass < 4; ++pass) { const int shift = 24 - 8 * pass;
;             if (tid < 256) hist[tid] = 0u;
;             __syncthreads();
; #pragma unroll
;             for (int j = 0; j < 8; ++j) if ((k[j] & mask) == prefix) atomicAdd((unsigned*)&hist[(k[j] >> shift) & 255u], 1u);
;             __syncthreads();
;             if (tid == 0) { unsigned cum = 0u; int d = 255; for (; d > 0; --d) { const unsigned hh = hist[d]; if (cum + hh >= want) break; cum += hh; } misc[0] = (unsigned)d; misc[1] = want - cum; }
;             __syncthreads();
;             prefix |= misc[0] << shift; mask |= 255u << shift; want = misc[1];
;             __syncthreads();
;         }
	s_and_saveexec_b64 s[2:3], s[40:41]
	s_cbranch_execz .LBB0_2211
	s_mov_b64 exec, -1
	v_mbcnt_lo_u32_b32 v102, -1, 0
	v_mbcnt_hi_u32_b32 v102, -1, v102
	v_lshlrev_b32_e32 v102, 4, v102
	ds_read_b128 v[104:107], v102
	s_waitcnt lgkmcnt(0)
	v_add_u32_e32 v108, v104, v105
	v_add3_u32 v108, v108, v106, v107
	s_nop 1
	v_add_u32_dpp v108, v108, v108 row_shl:1 row_mask:0xf bank_mask:0xf
	s_nop 1
	v_add_u32_dpp v108, v108, v108 row_shl:2 row_mask:0xf bank_mask:0xf
	s_nop 1
	v_add_u32_dpp v108, v108, v108 row_shl:4 row_mask:0xf bank_mask:0xf
	s_nop 1
	v_add_u32_dpp v108, v108, v108 row_shl:8 row_mask:0xf bank_mask:0xf
	s_nop 0
	v_readlane_b32 s5, v108, 16
	v_readlane_b32 s6, v108, 32
	v_readlane_b32 s7, v108, 48
	s_add_i32 s6, s6, s7
	s_add_i32 s5, s5, s6
	s_mov_b32 exec_lo, 0xffff
	s_mov_b32 exec_hi, 0
	v_add_u32_e32 v108, s5, v108
	s_mov_b32 exec_lo, 0xffff0000
	v_add_u32_e32 v108, s6, v108
	s_mov_b32 exec_lo, 0
	s_mov_b32 exec_hi, 0xffff
	v_add_u32_e32 v108, s7, v108
	s_mov_b64 exec, -1
	v_sub_u32_e32 v109, v108, v104
	v_sub_u32_e32 v110, v109, v105
	v_sub_u32_e32 v111, v110, v106
	v_cmp_le_u32_e64 s[4:5], s19, v108
	v_cmp_le_u32_e64 s[6:7], s19, v109
	v_cmp_le_u32_e64 s[8:9], s19, v110
	v_cmp_le_u32_e64 s[10:11], s19, v111
	s_andn2_b64 s[4:5], s[4:5], 1
	s_bcnt1_i32_b64 s4, s[4:5]
	s_bcnt1_i32_b64 s6, s[6:7]
	s_bcnt1_i32_b64 s8, s[8:9]
	s_bcnt1_i32_b64 s10, s[10:11]
	s_add_i32 s4, s4, s6
	s_add_i32 s8, s8, s10
	s_add_i32 s48, s4, s8
	s_add_i32 s5, s48, 1
	s_lshr_b32 s6, s5, 2
	s_and_b32 s7, s5, 3
	s_min_u32 s6, s6, 63
	v_readlane_b32 s8, v108, s6
	v_readlane_b32 s9, v109, s6
	v_readlane_b32 s10, v110, s6
	v_readlane_b32 s11, v111, s6
	s_cmp_eq_u32 s7, 1
	s_cselect_b32 s8, s9, s8
	s_cmp_eq_u32 s7, 2
	s_cselect_b32 s8, s10, s8
	s_cmp_eq_u32 s7, 3
	s_cselect_b32 s8, s11, s8
	s_cmp_gt_u32 s5, 0xff
	s_cselect_b32 s8, 0, s8
	s_sub_i32 s4, s19, s8
	s_mov_b64 exec, 1
	v_mov_b32_e32 v2, s48
	v_mov_b32_e32 v3, s4
	ds_write_b64 v147, v[2:3] offset:1024
.LBB0_2211:
	s_or_b64 exec, exec, s[2:3]
	s_waitcnt lgkmcnt(0)
	s_barrier
	ds_read_b64 v[2:3], v147 offset:1024
	s_waitcnt lgkmcnt(0)
	s_barrier
	v_readfirstlane_b32 s4, v2
	v_readfirstlane_b32 s19, v3
	s_and_saveexec_b64 s[2:3], s[38:39]
	ds_write_b32 v45, v147
	s_or_b64 exec, exec, s[2:3]
	s_lshl_b32 s2, s4, 8
	s_or_b32 s18, s2, s18
	v_and_b32_e32 v1, 0xffffff00, v11
	v_cmp_eq_u32_e32 vcc, s18, v1
	s_waitcnt lgkmcnt(0)
	s_barrier
	s_and_saveexec_b64 s[2:3], vcc
	v_and_b32_e32 v1, 0xff, v11
	v_lshl_add_u32 v1, v1, 2, 0
	ds_add_u32 v1, v181
	s_or_b64 exec, exec, s[2:3]
	v_and_b32_e32 v1, 0xffffff00, v10
	v_cmp_eq_u32_e32 vcc, s18, v1
	s_and_saveexec_b64 s[2:3], vcc
	v_and_b32_e32 v1, 0xff, v10
	v_lshl_add_u32 v1, v1, 2, 0
	ds_add_u32 v1, v181
	s_or_b64 exec, exec, s[2:3]
	v_and_b32_e32 v1, 0xffffff00, v9
	v_cmp_eq_u32_e32 vcc, s18, v1
	s_and_saveexec_b64 s[2:3], vcc
	v_and_b32_e32 v1, 0xff, v9
	v_lshl_add_u32 v1, v1, 2, 0
	ds_add_u32 v1, v181
	s_or_b64 exec, exec, s[2:3]
	v_and_b32_e32 v1, 0xffffff00, v8
	v_cmp_eq_u32_e32 vcc, s18, v1
	s_and_saveexec_b64 s[2:3], vcc
	v_and_b32_e32 v1, 0xff, v8
	v_lshl_add_u32 v1, v1, 2, 0
	ds_add_u32 v1, v181
	s_or_b64 exec, exec, s[2:3]
	v_and_b32_e32 v1, 0xffffff00, v7
	v_cmp_eq_u32_e32 vcc, s18, v1
	s_and_saveexec_b64 s[2:3], vcc
	v_and_b32_e32 v1, 0xff, v7
	v_lshl_add_u32 v1, v1, 2, 0
	ds_add_u32 v1, v181
	s_or_b64 exec, exec, s[2:3]
	v_and_b32_e32 v1, 0xffffff00, v6
	v_cmp_eq_u32_e32 vcc, s18, v1
	s_and_saveexec_b64 s[2:3], vcc
	v_and_b32_e32 v1, 0xff, v6
	v_lshl_add_u32 v1, v1, 2, 0
	ds_add_u32 v1, v181
	s_or_b64 exec, exec, s[2:3]
	v_and_b32_e32 v1, 0xffffff00, v5
	v_cmp_eq_u32_e32 vcc, s18, v1
	s_and_saveexec_b64 s[2:3], vcc
	v_and_b32_e32 v1, 0xff, v5
	v_lshl_add_u32 v1, v1, 2, 0
	ds_add_u32 v1, v181
	s_or_b64 exec, exec, s[2:3]
	v_and_b32_e32 v1, 0xffffff00, v4
	v_cmp_eq_u32_e32 vcc, s18, v1
	s_and_saveexec_b64 s[2:3], vcc
	v_and_b32_e32 v1, 0xff, v4
	v_lshl_add_u32 v1, v1, 2, 0
	ds_add_u32 v1, v181
	s_or_b64 exec, exec, s[2:3]
	s_waitcnt lgkmcnt(0)
	s_barrier
	s_and_saveexec_b64 s[2:3], s[40:41]
	s_cbranch_execz .LBB0_2252
	s_mov_b64 exec, -1
	v_mbcnt_lo_u32_b32 v102, -1, 0
	v_mbcnt_hi_u32_b32 v102, -1, v102
	v_lshlrev_b32_e32 v102, 4, v102
	ds_read_b128 v[104:107], v102
	s_waitcnt lgkmcnt(0)
	v_add_u32_e32 v108, v104, v105
	v_add3_u32 v108, v108, v106, v107
	s_nop 1
	v_add_u32_dpp v108, v108, v108 row_shl:1 row_mask:0xf bank_mask:0xf
	s_nop 1
	v_add_u32_dpp v108, v108, v108 row_shl:2 row_mask:0xf bank_mask:0xf
	s_nop 1
	v_add_u32_dpp v108, v108, v108 row_shl:4 row_mask:0xf bank_mask:0xf
	s_nop 1
	v_add_u32_dpp v108, v108, v108 row_shl:8 row_mask:0xf bank_mask:0xf
	s_nop 0
	v_readlane_b32 s5, v108, 16
	v_readlane_b32 s6, v108, 32
	v_readlane_b32 s7, v108, 48
	s_add_i32 s6, s6, s7
	s_add_i32 s5, s5, s6
	s_mov_b32 exec_lo, 0xffff
	s_mov_b32 exec_hi, 0
	v_add_u32_e32 v108, s5, v108
	s_mov_b32 exec_lo, 0xffff0000
	v_add_u32_e32 v108, s6, v108
	s_mov_b32 exec_lo, 0
	s_mov_b32 exec_hi, 0xffff
	v_add_u32_e32 v108, s7, v108
	s_mov_b64 exec, -1
	v_sub_u32_e32 v109, v108, v104
	v_sub_u32_e32 v110, v109, v105
	v_sub_u32_e32 v111, v110, v106
	v_cmp_le_u32_e64 s[4:5], s19, v108
	v_cmp_le_u32_e64 s[6:7], s19, v109
	v_cmp_le_u32_e64 s[8:9], s19, v110
	v_cmp_le_u32_e64 s[10:11], s19, v111
	s_andn2_b64 s[4:5], s[4:5], 1
	s_bcnt1_i32_b64 s4, s[4:5]
	s_bcnt1_i32_b64 s6, s[6:7]
	s_bcnt1_i32_b64 s8, s[8:9]
	s_bcnt1_i32_b64 s10, s[10:11]
	s_add_i32 s4, s4, s6
	s_add_i32 s8, s8, s10
	s_add_i32 s48, s4, s8
	s_add_i32 s5, s48, 1
	s_lshr_b32 s6, s5, 2
	s_and_b32 s7, s5, 3
	s_min_u32 s6, s6, 63
	v_readlane_b32 s8, v108, s6
	v_readlane_b32 s9, v109, s6
	v_readlane_b32 s10, v110, s6
	v_readlane_b32 s11, v111, s6
	s_cmp_eq_u32 s7, 1
	s_cselect_b32 s8, s9, s8
	s_cmp_eq_u32 s7, 2
	s_cselect_b32 s8, s10, s8
	s_cmp_eq_u32 s7, 3
	s_cselect_b32 s8, s11, s8
	s_cmp_gt_u32 s5, 0xff
	s_cselect_b32 s8, 0, s8
	s_sub_i32 s4, s19, s8
	s_mov_b64 exec, 1
	v_mov_b32_e32 v2, s48
	v_mov_b32_e32 v3, s4
	ds_write_b64 v147, v[2:3] offset:1024
